# MFMA/LDS interleave at the PV segment head (attention inst 1): the first eight V-fragment ds_read_b64_tr are issued as soon as the P conversions free their destination registers instead of after all 1
# baseline (speedup 1.0000x reference)
.LBB0_813:
	v_cvt_pk_bf16_f32 v66, v66, v67
	v_cvt_pk_bf16_f32 v67, v68, v69
	v_cvt_pk_bf16_f32 v68, v70, v71
	v_cvt_pk_bf16_f32 v69, v72, v83
	v_cvt_pk_bf16_f32 v70, v73, v74
	v_cvt_pk_bf16_f32 v71, v75, v76
	v_cvt_pk_bf16_f32 v72, v77, v78
	v_cvt_pk_bf16_f32 v73, v80, v81
	v_lshl_add_u32 v78, s87, 14, v172
	ds_read_b64_tr_b16 v[74:75], v78 offset:0
	ds_read_b64_tr_b16 v[76:77], v78 offset:0x800
	ds_read_b64_tr_b16 v[80:81], v78 offset:0x1000
	v_cvt_pk_bf16_f32 v178, v82, v175
	v_cvt_pk_bf16_f32 v179, v84, v85
	v_cvt_pk_bf16_f32 v180, v86, v87
	v_cvt_pk_bf16_f32 v181, v88, v176
	ds_read_b64_tr_b16 v[82:83], v78 offset:0x1800
	v_cvt_pk_bf16_f32 v84, v89, v90
	v_cvt_pk_bf16_f32 v85, v91, v92
	v_cvt_pk_bf16_f32 v86, v93, v94
	v_cvt_pk_bf16_f32 v87, v95, v96
	ds_read_b64_tr_b16 v[88:89], v78 offset:0x2000
	ds_read_b64_tr_b16 v[90:91], v78 offset:0x2800
	ds_read_b64_tr_b16 v[92:93], v78 offset:0x3000
	ds_read_b64_tr_b16 v[94:95], v78 offset:0x3800


	v_fmac_f32_e32 v79, v174, v97
	ds_read_b64_tr_b16 v[174:175], v78 offset:0x200
	ds_read_b64_tr_b16 v[176:177], v78 offset:0xa00
	ds_read_b64_tr_b16 v[182:183], v78 offset:0x1200
	ds_read_b64_tr_b16 v[184:185], v78 offset:0x1a00
	ds_read_b64_tr_b16 v[186:187], v78 offset:0x2200
	ds_read_b64_tr_b16 v[188:189], v78 offset:0x2a00
	ds_read_b64_tr_b16 v[190:191], v78 offset:0x3200
	ds_read_b64_tr_b16 v[192:193], v78 offset:0x3a00
	s_waitcnt lgkmcnt(8)


	v_mfma_f32_32x32x16_bf16 v[50:65], v[178:181], v[74:77], v[50:65]
	ds_read_b64_tr_b16 v[74:75], v78 offset:0x400
	ds_read_b64_tr_b16 v[76:77], v78 offset:0xc00
	v_mfma_f32_32x32x16_bf16 v[50:65], v[84:87], v[80:83], v[50:65]
	ds_read_b64_tr_b16 v[80:81], v78 offset:0x1400
	ds_read_b64_tr_b16 v[82:83], v78 offset:0x1c00
	v_mfma_f32_32x32x16_bf16 v[50:65], v[66:69], v[88:91], v[50:65]
	ds_read_b64_tr_b16 v[88:89], v78 offset:0x2400
	ds_read_b64_tr_b16 v[90:91], v78 offset:0x2c00
	v_mfma_f32_32x32x16_bf16 v[50:65], v[70:73], v[92:95], v[50:65]
	ds_read_b64_tr_b16 v[92:93], v78 offset:0x3400
	ds_read_b64_tr_b16 v[94:95], v78 offset:0x3c00
	s_waitcnt lgkmcnt(8)
	v_mfma_f32_32x32x16_bf16 v[34:49], v[178:181], v[174:177], v[34:49]
	ds_read_b64_tr_b16 v[174:175], v78 offset:0x600
	ds_read_b64_tr_b16 v[176:177], v78 offset:0xe00
	v_mfma_f32_32x32x16_bf16 v[34:49], v[84:87], v[182:185], v[34:49]
	ds_read_b64_tr_b16 v[182:183], v78 offset:0x1600
	ds_read_b64_tr_b16 v[184:185], v78 offset:0x1e00
	v_mfma_f32_32x32x16_bf16 v[34:49], v[66:69], v[186:189], v[34:49]
	ds_read_b64_tr_b16 v[186:187], v78 offset:0x2600
	ds_read_b64_tr_b16 v[188:189], v78 offset:0x2e00
	v_mfma_f32_32x32x16_bf16 v[34:49], v[70:73], v[190:193], v[34:49]
	ds_read_b64_tr_b16 v[190:191], v78 offset:0x3600
	ds_read_b64_tr_b16 v[192:193], v78 offset:0x3e00
	s_waitcnt lgkmcnt(8)
	v_mfma_f32_32x32x16_bf16 v[18:33], v[178:181], v[74:77], v[18:33]
	s_waitcnt lgkmcnt(0)
	v_mfma_f32_32x32x16_bf16 v[18:33], v[84:87], v[80:83], v[18:33]
	v_mfma_f32_32x32x16_bf16 v[18:33], v[66:69], v[88:91], v[18:33]
	v_mfma_f32_32x32x16_bf16 v[18:33], v[70:73], v[92:95], v[18:33]
	v_mfma_f32_32x32x16_bf16 v[2:17], v[178:181], v[174:177], v[2:17]
	s_add_i32 s86, s86, 64
	s_add_i32 s12, s12, 1
	s_add_u32 s94, s94, s16
	s_addc_u32 s95, s95, s17
	s_add_u32 s96, s96, s14
	s_addc_u32 s97, s97, s15


	v_mfma_f32_32x32x16_bf16 v[2:17], v[84:87], v[182:185], v[2:17]
	v_subrev_u32_e32 v168, 64, v168
	s_cmp_eq_u32 s83, s86
	v_mfma_f32_32x32x16_bf16 v[2:17], v[66:69], v[186:189], v[2:17]
	v_mfma_f32_32x32x16_bf16 v[2:17], v[70:73], v[190:193], v[2:17]
	s_cbranch_scc1 .LBB0_815
	v_mov_b32_e32 v174, v79
	s_add_i32 s56, s86, 0xe0
	s_cmp_ge_i32 s56, s84
	s_cbranch_scc0 .LBB0_805
